# moe_tables: the 16 per-thread BCNT loads issued as two batches of eight (were 8 dependent round trips); on top of bias1 + unscaled fp8 MFMA
# speedup vs baseline: 1.0088x; 1.0045x over previous
.LBB0_1609:
	v_mbcnt_lo_u32_b32 v0, -1, 0
	v_mbcnt_hi_u32_b32 v0, -1, v0
	s_movk_i32 s4, 0x100
	v_or_b32_e32 v12, s33, v0
	v_ashrrev_i32_e32 v4, 5, v12
	v_mov_b32_e32 v5, 0
	v_and_b32_e32 v0, 31, v0
	v_cmp_gt_i32_e32 vcc, s4, v4
	v_mov_b32_e32 v8, 0
	s_and_saveexec_b64 s[34:35], vcc
	s_cbranch_execz .LBB0_1621
	v_lshl_add_u32 v6, v4, 5, v0
	v_lshlrev_b32_e32 v6, 2, v6
	v_sub_u32_e32 v7, s20, v4
	s_mov_b64 s[38:39], s[8:9]
	global_load_dword v13, v6, s[38:39]
	global_load_dword v14, v6, s[38:39] offset:2048
	s_add_u32 s38, s38, 0x1000
	s_addc_u32 s39, s39, 0
	global_load_dword v15, v6, s[38:39]
	global_load_dword v16, v6, s[38:39] offset:2048
	s_add_u32 s38, s38, 0x1000
	s_addc_u32 s39, s39, 0
	global_load_dword v17, v6, s[38:39]
	global_load_dword v18, v6, s[38:39] offset:2048
	s_add_u32 s38, s38, 0x1000
	s_addc_u32 s39, s39, 0
	global_load_dword v19, v6, s[38:39]
	global_load_dword v20, v6, s[38:39] offset:2048
	s_add_u32 s38, s38, 0x1000
	s_addc_u32 s39, s39, 0
	s_waitcnt vmcnt(0)
	v_add_u32_e32 v8, v8, v13
	v_cmp_lt_i32_e32 vcc, 0, v7
	s_nop 1
	v_cndmask_b32_e32 v9, 0, v13, vcc
	v_add_u32_e32 v5, v5, v9
	v_add_u32_e32 v8, v8, v14
	v_cmp_lt_i32_e32 vcc, 16, v7
	s_nop 1
	v_cndmask_b32_e32 v9, 0, v14, vcc
	v_add_u32_e32 v5, v5, v9
	v_add_u32_e32 v8, v8, v15
	v_cmp_lt_i32_e32 vcc, 32, v7
	s_nop 1
	v_cndmask_b32_e32 v9, 0, v15, vcc
	v_add_u32_e32 v5, v5, v9
	v_add_u32_e32 v8, v8, v16
	v_cmp_lt_i32_e32 vcc, 48, v7
	s_nop 1
	v_cndmask_b32_e32 v9, 0, v16, vcc
	v_add_u32_e32 v5, v5, v9
	v_add_u32_e32 v8, v8, v17
	v_cmp_lt_i32_e32 vcc, 64, v7
	s_nop 1
	v_cndmask_b32_e32 v9, 0, v17, vcc
	v_add_u32_e32 v5, v5, v9
	v_add_u32_e32 v8, v8, v18
	v_cmp_lt_i32_e32 vcc, 0x50, v7
	s_nop 1
	v_cndmask_b32_e32 v9, 0, v18, vcc
	v_add_u32_e32 v5, v5, v9
	v_add_u32_e32 v8, v8, v19
	v_cmp_lt_i32_e32 vcc, 0x60, v7
	s_nop 1
	v_cndmask_b32_e32 v9, 0, v19, vcc
	v_add_u32_e32 v5, v5, v9
	v_add_u32_e32 v8, v8, v20
	v_cmp_lt_i32_e32 vcc, 0x70, v7
	s_nop 1
	v_cndmask_b32_e32 v9, 0, v20, vcc
	v_add_u32_e32 v5, v5, v9
	global_load_dword v13, v6, s[38:39]
	global_load_dword v14, v6, s[38:39] offset:2048
	s_add_u32 s38, s38, 0x1000
	s_addc_u32 s39, s39, 0
	global_load_dword v15, v6, s[38:39]
	global_load_dword v16, v6, s[38:39] offset:2048
	s_add_u32 s38, s38, 0x1000
	s_addc_u32 s39, s39, 0
	global_load_dword v17, v6, s[38:39]
	global_load_dword v18, v6, s[38:39] offset:2048
	s_add_u32 s38, s38, 0x1000
	s_addc_u32 s39, s39, 0
	global_load_dword v19, v6, s[38:39]
	global_load_dword v20, v6, s[38:39] offset:2048
	s_add_u32 s38, s38, 0x1000
	s_addc_u32 s39, s39, 0
	s_waitcnt vmcnt(0)
	v_add_u32_e32 v8, v8, v13
	v_cmp_lt_i32_e32 vcc, 0x80, v7
	s_nop 1
	v_cndmask_b32_e32 v9, 0, v13, vcc
	v_add_u32_e32 v5, v5, v9
	v_add_u32_e32 v8, v8, v14
	v_cmp_lt_i32_e32 vcc, 0x90, v7
	s_nop 1
	v_cndmask_b32_e32 v9, 0, v14, vcc
	v_add_u32_e32 v5, v5, v9
	v_add_u32_e32 v8, v8, v15
	v_cmp_lt_i32_e32 vcc, 0xa0, v7
	s_nop 1
	v_cndmask_b32_e32 v9, 0, v15, vcc
	v_add_u32_e32 v5, v5, v9
	v_add_u32_e32 v8, v8, v16
	v_cmp_lt_i32_e32 vcc, 0xb0, v7
	s_nop 1
	v_cndmask_b32_e32 v9, 0, v16, vcc
	v_add_u32_e32 v5, v5, v9
	v_add_u32_e32 v8, v8, v17
	v_cmp_lt_i32_e32 vcc, 0xc0, v7
	s_nop 1
	v_cndmask_b32_e32 v9, 0, v17, vcc
	v_add_u32_e32 v5, v5, v9
	v_add_u32_e32 v8, v8, v18
	v_cmp_lt_i32_e32 vcc, 0xd0, v7
	s_nop 1
	v_cndmask_b32_e32 v9, 0, v18, vcc
	v_add_u32_e32 v5, v5, v9
	v_add_u32_e32 v8, v8, v19
	v_cmp_lt_i32_e32 vcc, 0xe0, v7
	s_nop 1
	v_cndmask_b32_e32 v9, 0, v19, vcc
	v_add_u32_e32 v5, v5, v9
	v_add_u32_e32 v8, v8, v20
	v_cmp_lt_i32_e32 vcc, 0xf0, v7
	s_nop 1
	v_cndmask_b32_e32 v9, 0, v20, vcc
	v_add_u32_e32 v5, v5, v9
